# P1: next row's x requested into a second register bank before the current row is reduced
# speedup vs baseline: 1.0084x; 1.0084x over previous
; __device__ __forceinline__ void phase1(const Args& a, int lane, int wave, int vcu, int G) {
;     ...
;     for (int m = vcu * 8 + wave; m < MROWS; m += G * 8) {
;         const float* xr = m < NT ? a.in[0] + (size_t)m * 2048 : a.in[2] + (size_t)(m - NT) * 2048;
;         const float* mr = mod + (size_t)(m < NT ? (m >> 11) : 8) * 12288;
;         f32x4 v[8]; float ss = 0.f;
; #pragma unroll
;         for (int j = 0; j < 8; ++j) { v[j] = __builtin_nontemporal_load((const f32x4*)(xr + 4 * (lane + 64 * j))); ss += v[j][0] * v[j][0] + v[j][1] * v[j][1] + v[j][2] * v[j][2] + v[j][3] * v[j][3]; }
;         const float rstd = rsqrtf(wave_sum(ss) * (1.f / 2048.f) + EPS);
; #pragma unroll
;         for (int j = 0; j < 8; ++j) { const int c = 4 * (lane + 64 * j); const f32x4 gg = *(const f32x4*)(g + c), sh = *(const f32x4*)(mr + c), sc = *(const f32x4*)(mr + 2048 + c);
.LBB0_87:
	s_cmp_gt_i32 s94, 1
	s_cselect_b64 s[0:1], -1, 0
	s_cmp_lt_i32 s95, 2
	s_cselect_b64 s[2:3], -1, 0
	s_or_b64 s[0:1], s[0:1], s[2:3]
	s_and_b64 vcc, exec, s[0:1]
	s_cbranch_vccnz .LBB0_143
	v_mov_b32_e32 v1, v0
	s_nop 0
	v_readfirstlane_b32 s0, v1
	s_ashr_i32 s1, s0, 6
	v_readlane_b32 s0, v246, 2
	s_lshl_b32 s2, s0, 3
	s_add_i32 s0, s1, s2
	s_cmpk_gt_i32 s0, 0x47ff
	s_cbranch_scc1 .LBB0_93
	v_lshlrev_b32_e32 v1, 2, v1
	v_and_b32_e32 v2, 0xfc, v1
	v_mov_b32_e32 v5, 0
	v_lshlrev_b32_e32 v4, 2, v2
	v_or_b32_e32 v12, 0x400, v2
	s_waitcnt lgkmcnt(0)
	v_lshl_add_u64 v[26:27], s[80:81], 0, v[4:5]
	v_or_b32_e32 v14, 0x500, v2
	v_lshlrev_b32_e32 v4, 2, v12
	v_or_b32_e32 v16, 0x600, v2
	v_lshl_add_u64 v[28:29], s[80:81], 0, v[4:5]
	v_lshlrev_b32_e32 v4, 2, v14
	v_or_b32_e32 v18, 0x700, v2
	v_lshl_add_u64 v[30:31], s[80:81], 0, v[4:5]
	v_lshlrev_b32_e32 v4, 2, v16
	v_lshl_add_u64 v[32:33], s[80:81], 0, v[4:5]
	v_lshlrev_b32_e32 v4, 2, v18
	v_lshl_add_u64 v[34:35], s[80:81], 0, v[4:5]
	v_lshlrev_b32_e32 v4, 1, v2
	s_add_u32 s16, s92, 0x100000
	v_lshl_add_u64 v[4:5], s[92:93], 0, v[4:5]
	s_mov_b64 s[4:5], 0x1a200000
	s_addc_u32 s17, s93, 0
	s_lshl_b32 s0, s97, 3
	v_lshl_add_u64 v[36:37], v[4:5], 0, s[4:5]
	s_ashr_i32 s3, s1, 31
	s_ashr_i32 s5, s2, 31
	s_add_u32 s4, s1, s2
	s_addc_u32 s5, s3, s5
	s_ashr_i32 s1, s0, 31
	s_lshl_b64 s[2:3], s[4:5], 13
	v_or_b32_e32 v6, 0x100, v2
	v_or_b32_e32 v8, 0x200, v2
	v_or_b32_e32 v10, 0x300, v2
	s_add_u32 s6, s68, s2
	s_addc_u32 s7, s69, s3
	s_lshl_b64 s[8:9], s[0:1], 13
	s_mov_b32 s11, 0
	v_lshlrev_b32_e32 v1, 2, v2
	v_lshlrev_b32_e32 v41, 2, v12
	v_lshlrev_b32_e32 v42, 2, v14
	v_lshlrev_b32_e32 v43, 2, v16
	v_lshlrev_b32_e32 v44, 2, v18
	v_mov_b32_e32 v45, 0x358637bd
	v_mov_b32_e32 v46, 0x3a000000
	s_mov_b32 s18, 0x800000
	s_movk_i32 s19, 0x7fff
	s_mov_b32 s20, 0xffff0000
	v_lshlrev_b32_e32 v47, 2, v6
	v_lshlrev_b32_e32 v48, 2, v8
	v_lshlrev_b32_e32 v49, 2, v10
	global_load_dwordx4 v[90:93], v[26:27], off
	global_load_dwordx4 v[94:97], v[26:27], off offset:1024
	global_load_dwordx4 v[98:101], v[26:27], off offset:2048
	global_load_dwordx4 v[102:105], v[26:27], off offset:3072
	global_load_dwordx4 v[106:109], v[28:29], off
	global_load_dwordx4 v[110:113], v[30:31], off
	global_load_dwordx4 v[114:117], v[32:33], off
	global_load_dwordx4 v[118:121], v[34:35], off
	s_cmpk_lt_i32 s4, 0x4000
	s_mov_b64 s[12:13], s[6:7]
	s_cbranch_scc1 .Lp1_lat_a
	s_add_i32 s26, s4, 0xffffc000
	s_mov_b32 s27, 0
	s_lshl_b64 s[26:27], s[26:27], 13
	s_add_u32 s12, s72, s26
	s_addc_u32 s13, s73, s27

; __device__ __forceinline__ void phase1(const Args& a, int lane, int wave, int vcu, int G) {
;     ...
;     for (int m = vcu * 8 + wave; m < MROWS; m += G * 8) {
;         const float* xr = m < NT ? a.in[0] + (size_t)m * 2048 : a.in[2] + (size_t)(m - NT) * 2048;
;         const float* mr = mod + (size_t)(m < NT ? (m >> 11) : 8) * 12288;
;         f32x4 v[8]; float ss = 0.f;
; #pragma unroll
;         for (int j = 0; j < 8; ++j) { v[j] = __builtin_nontemporal_load((const f32x4*)(xr + 4 * (lane + 64 * j))); ss += v[j][0] * v[j][0] + v[j][1] * v[j][1] + v[j][2] * v[j][2] + v[j][3] * v[j][3]; }
;         const float rstd = rsqrtf(wave_sum(ss) * (1.f / 2048.f) + EPS);
; #pragma unroll
;         for (int j = 0; j < 8; ++j) { const int c = 4 * (lane + 64 * j); const f32x4 gg = *(const f32x4*)(g + c), sh = *(const f32x4*)(mr + c), sc = *(const f32x4*)(mr + 2048 + c);
;             const f32x4 o = v[j] * rstd * gg * (sc + 1.f) + sh;
.Lp1_top:
	s_min_i32 s10, s4, 0x4000
	s_ashr_i32 s10, s10, 11
	s_mul_hi_i32 s13, s10, 0xc000
	s_mul_i32 s10, s10, 0xc000
	s_add_u32 s12, s16, s10
	s_addc_u32 s13, s17, s13
	s_add_u32 s14, s12, 0x2000
	s_addc_u32 s15, s13, 0
	global_load_dwordx4 v[122:125], v1, s[14:15]
	global_load_dwordx4 v[126:129], v1, s[14:15] offset:1024
	global_load_dwordx4 v[130:133], v1, s[14:15] offset:2048
	global_load_dwordx4 v[134:137], v1, s[14:15] offset:3072
	global_load_dwordx4 v[138:141], v41, s[14:15]
	global_load_dwordx4 v[142:145], v42, s[14:15]
	global_load_dwordx4 v[146:149], v43, s[14:15]
	global_load_dwordx4 v[150:153], v44, s[14:15]
	global_load_dwordx4 v[154:157], v1, s[12:13]
	global_load_dwordx4 v[158:161], v1, s[12:13] offset:1024
	global_load_dwordx4 v[162:165], v1, s[12:13] offset:2048
	global_load_dwordx4 v[166:169], v1, s[12:13] offset:3072
	global_load_dwordx4 v[170:173], v41, s[12:13]
	global_load_dwordx4 v[174:177], v42, s[12:13]
	global_load_dwordx4 v[178:181], v43, s[12:13]
	global_load_dwordx4 v[182:185], v44, s[12:13]
	v_mov_b32_e32 v40, 0
	v_mov_b32_e32 v84, 0
	s_lshl_b64 s[2:3], s[4:5], 12
	s_add_u32 s4, s4, s0
	s_addc_u32 s5, s5, s1
	s_add_u32 s6, s6, s8
	s_addc_u32 s7, s7, s9
	s_cmpk_lt_i32 s4, 0x4800
	s_cselect_b32 s21, 1, 0
	s_cbranch_scc0 .Lp1_last_a
	s_cmpk_lt_i32 s4, 0x4000
	s_mov_b64 s[24:25], s[6:7]
	s_cbranch_scc1 .Lp1_lat_b1
	s_add_i32 s26, s4, 0xffffc000
	s_mov_b32 s27, 0
	s_lshl_b64 s[26:27], s[26:27], 13
	s_add_u32 s24, s72, s26
	s_addc_u32 s25, s73, s27
.Lp1_lat_b1:
	global_load_dwordx4 v[186:189], v1, s[24:25] nt
	global_load_dwordx4 v[190:193], v1, s[24:25] offset:1024 nt
	global_load_dwordx4 v[194:197], v1, s[24:25] offset:2048 nt
	global_load_dwordx4 v[198:201], v1, s[24:25] offset:3072 nt
	global_load_dwordx4 v[202:205], v41, s[24:25] nt
	global_load_dwordx4 v[206:209], v42, s[24:25] nt
	global_load_dwordx4 v[210:213], v43, s[24:25] nt
	global_load_dwordx4 v[214:217], v44, s[24:25] nt
	s_waitcnt vmcnt(24)
	s_branch .Lp1_red_a
.Lp1_last_a:
	s_waitcnt vmcnt(16)
.Lp1_red_a:
	v_mul_f32_e32 v85, v50, v50
	v_mul_f32_e32 v86, v54, v54
	v_mul_f32_e32 v87, v22, v22
	v_mul_f32_e32 v88, v18, v18
	v_fmac_f32_e32 v85, v51, v51
	v_fmac_f32_e32 v86, v55, v55
	v_fmac_f32_e32 v87, v23, v23
	v_fmac_f32_e32 v88, v19, v19
	v_fmac_f32_e32 v85, v52, v52
	v_fmac_f32_e32 v86, v56, v56
	v_fmac_f32_e32 v87, v24, v24
	v_fmac_f32_e32 v88, v20, v20
	v_fmac_f32_e32 v85, v53, v53
	v_fmac_f32_e32 v86, v57, v57
	v_fmac_f32_e32 v87, v25, v25
	v_fmac_f32_e32 v88, v21, v21
	v_fmac_f32_e32 v85, v14, v14
	v_fmac_f32_e32 v86, v10, v10
	v_fmac_f32_e32 v87, v6, v6
	v_fmac_f32_e32 v88, v2, v2
	v_fmac_f32_e32 v85, v15, v15
	v_fmac_f32_e32 v86, v11, v11
	v_fmac_f32_e32 v87, v7, v7
	v_fmac_f32_e32 v88, v3, v3
	v_fmac_f32_e32 v85, v16, v16
	v_fmac_f32_e32 v86, v12, v12
	v_fmac_f32_e32 v87, v8, v8
	v_fmac_f32_e32 v88, v4, v4
	v_fmac_f32_e32 v85, v17, v17
	v_fmac_f32_e32 v86, v13, v13
	v_fmac_f32_e32 v87, v9, v9
	v_fmac_f32_e32 v88, v5, v5
	v_add_f32_e32 v85, v85, v86
	v_add_f32_e32 v87, v87, v88
	v_add_f32_e32 v38, v85, v87
	s_nop 1
	v_add_f32_dpp v38, v38, v38 row_shr:1 row_mask:0xf bank_mask:0xf bound_ctrl:1
	s_nop 1
	v_add_f32_dpp v38, v38, v38 row_shr:2 row_mask:0xf bank_mask:0xf bound_ctrl:1
	s_nop 1
	v_add_f32_dpp v38, v38, v38 row_shr:4 row_mask:0xf bank_mask:0xf bound_ctrl:1
	s_nop 1
	v_add_f32_dpp v38, v38, v38 row_shr:8 row_mask:0xf bank_mask:0xf bound_ctrl:1
	s_nop 1
	v_mov_b32_dpp v40, v38 row_bcast:15 row_mask:0xa bank_mask:0xf
	v_add_f32_e32 v38, v38, v40
	s_nop 1
	v_mov_b32_dpp v84, v38 row_bcast:31 row_mask:0xc bank_mask:0xf
	v_add_f32_e32 v38, v38, v84
	s_nop 0
	v_readlane_b32 s10, v38, 63
	s_nop 1
	v_fma_f32 v38, s10, v46, v45
	v_mul_f32_e32 v39, 0x4b800000, v38
	v_cmp_gt_f32_e32 vcc, s18, v38
	s_nop 1
	v_cndmask_b32_e32 v38, v38, v39, vcc
	v_rsq_f32_e32 v40, v38
	v_lshl_add_u64 v[38:39], v[36:37], 0, s[2:3]
	v_mul_f32_e32 v70, 0x45800000, v40
	v_cndmask_b32_e32 v40, v40, v70, vcc
	v_pk_mul_f32 v[50:51], v[50:51], v[40:41] op_sel_hi:[1,0]
	v_pk_mul_f32 v[52:53], v[52:53], v[40:41] op_sel_hi:[1,0]
	v_pk_mul_f32 v[54:55], v[54:55], v[40:41] op_sel_hi:[1,0]
	v_pk_mul_f32 v[56:57], v[56:57], v[40:41] op_sel_hi:[1,0]
	v_pk_mul_f32 v[22:23], v[22:23], v[40:41] op_sel_hi:[1,0]
	v_pk_mul_f32 v[24:25], v[24:25], v[40:41] op_sel_hi:[1,0]
	v_pk_mul_f32 v[18:19], v[18:19], v[40:41] op_sel_hi:[1,0]
	v_pk_mul_f32 v[20:21], v[20:21], v[40:41] op_sel_hi:[1,0]
	v_pk_mul_f32 v[14:15], v[14:15], v[40:41] op_sel_hi:[1,0]
	v_pk_mul_f32 v[16:17], v[16:17], v[40:41] op_sel_hi:[1,0]
	v_pk_mul_f32 v[10:11], v[10:11], v[40:41] op_sel_hi:[1,0]
	v_pk_mul_f32 v[12:13], v[12:13], v[40:41] op_sel_hi:[1,0]
	v_pk_mul_f32 v[6:7], v[6:7], v[40:41] op_sel_hi:[1,0]
	v_pk_mul_f32 v[8:9], v[8:9], v[40:41] op_sel_hi:[1,0]
	v_pk_mul_f32 v[2:3], v[2:3], v[40:41] op_sel_hi:[1,0]
	v_pk_mul_f32 v[4:5], v[4:5], v[40:41] op_sel_hi:[1,0]
	v_pk_mul_f32 v[50:51], v[90:91], v[50:51]
	v_pk_mul_f32 v[52:53], v[92:93], v[52:53]
	v_pk_mul_f32 v[54:55], v[94:95], v[54:55]
	v_pk_mul_f32 v[56:57], v[96:97], v[56:57]
	v_pk_mul_f32 v[22:23], v[98:99], v[22:23]
	v_pk_mul_f32 v[24:25], v[100:101], v[24:25]
	v_pk_mul_f32 v[18:19], v[102:103], v[18:19]
	v_pk_mul_f32 v[20:21], v[104:105], v[20:21]
	v_pk_mul_f32 v[14:15], v[106:107], v[14:15]
	v_pk_mul_f32 v[16:17], v[108:109], v[16:17]
	v_pk_mul_f32 v[10:11], v[110:111], v[10:11]
	v_pk_mul_f32 v[12:13], v[112:113], v[12:13]
	v_pk_mul_f32 v[6:7], v[114:115], v[6:7]
	v_pk_mul_f32 v[8:9], v[116:117], v[8:9]
	v_pk_mul_f32 v[2:3], v[118:119], v[2:3]
	v_pk_mul_f32 v[4:5], v[120:121], v[4:5]
	s_cmp_lg_u32 s21, 0
	s_cbranch_scc1 .Lp1_w8_a
	s_waitcnt vmcnt(0)
	s_branch .Lp1_mod_a
; __device__ __forceinline__ unsigned pk2(float lo, float hi) { return f2bf(lo) | (f2bf(hi) << 16); }
; __device__ __forceinline__ void phase1(const Args& a, int lane, int wave, int vcu, int G) {
;     ...
;         for (int j = 0; j < 8; ++j) { const int c = 4 * (lane + 64 * j); const f32x4 gg = *(const f32x4*)(g + c), sh = *(const f32x4*)(mr + c), sc = *(const f32x4*)(mr + 2048 + c);
;             const f32x4 o = v[j] * rstd * gg * (sc + 1.f) + sh;
;             v2u q; q.x = pk2(o[0], o[1]); q.y = pk2(o[2], o[3]); *(v2u*)(H + (size_t)m * 2048 + c) = q; }
.Lp1_w8_a:
	s_waitcnt vmcnt(8)
.Lp1_mod_a:
	v_pk_add_f32 v[122:123], v[122:123], 1.0 op_sel_hi:[1,0]
	v_pk_add_f32 v[124:125], v[124:125], 1.0 op_sel_hi:[1,0]
	v_pk_fma_f32 v[50:51], v[122:123], v[50:51], v[154:155]
	v_pk_fma_f32 v[52:53], v[124:125], v[52:53], v[156:157]
	v_cvt_pk_bf16_f32 v50, v50, v51
	v_cvt_pk_bf16_f32 v51, v52, v53
	global_store_dwordx2 v[38:39], v[50:51], off
	v_pk_add_f32 v[126:127], v[126:127], 1.0 op_sel_hi:[1,0]
	v_pk_add_f32 v[128:129], v[128:129], 1.0 op_sel_hi:[1,0]
	v_pk_fma_f32 v[54:55], v[126:127], v[54:55], v[158:159]
	v_pk_fma_f32 v[56:57], v[128:129], v[56:57], v[160:161]
	v_cvt_pk_bf16_f32 v54, v54, v55
	v_cvt_pk_bf16_f32 v55, v56, v57
	global_store_dwordx2 v[38:39], v[54:55], off offset:512
	v_pk_add_f32 v[130:131], v[130:131], 1.0 op_sel_hi:[1,0]
	v_pk_add_f32 v[132:133], v[132:133], 1.0 op_sel_hi:[1,0]
	v_pk_fma_f32 v[22:23], v[130:131], v[22:23], v[162:163]
	v_pk_fma_f32 v[24:25], v[132:133], v[24:25], v[164:165]
	v_cvt_pk_bf16_f32 v22, v22, v23
	v_cvt_pk_bf16_f32 v23, v24, v25
	global_store_dwordx2 v[38:39], v[22:23], off offset:1024
	v_pk_add_f32 v[134:135], v[134:135], 1.0 op_sel_hi:[1,0]
	v_pk_add_f32 v[136:137], v[136:137], 1.0 op_sel_hi:[1,0]
	v_pk_fma_f32 v[18:19], v[134:135], v[18:19], v[166:167]
	v_pk_fma_f32 v[20:21], v[136:137], v[20:21], v[168:169]
	v_cvt_pk_bf16_f32 v18, v18, v19
	v_cvt_pk_bf16_f32 v19, v20, v21
	global_store_dwordx2 v[38:39], v[18:19], off offset:1536
	v_pk_add_f32 v[138:139], v[138:139], 1.0 op_sel_hi:[1,0]
	v_pk_add_f32 v[140:141], v[140:141], 1.0 op_sel_hi:[1,0]
	v_pk_fma_f32 v[14:15], v[138:139], v[14:15], v[170:171]
	v_pk_fma_f32 v[16:17], v[140:141], v[16:17], v[172:173]
	v_cvt_pk_bf16_f32 v14, v14, v15
	v_cvt_pk_bf16_f32 v15, v16, v17
	global_store_dwordx2 v[38:39], v[14:15], off offset:2048
	v_pk_add_f32 v[142:143], v[142:143], 1.0 op_sel_hi:[1,0]
	v_pk_add_f32 v[144:145], v[144:145], 1.0 op_sel_hi:[1,0]
	v_pk_fma_f32 v[10:11], v[142:143], v[10:11], v[174:175]
	v_pk_fma_f32 v[12:13], v[144:145], v[12:13], v[176:177]
	v_cvt_pk_bf16_f32 v10, v10, v11
	v_cvt_pk_bf16_f32 v11, v12, v13
	global_store_dwordx2 v[38:39], v[10:11], off offset:2560
	v_pk_add_f32 v[146:147], v[146:147], 1.0 op_sel_hi:[1,0]
	v_pk_add_f32 v[148:149], v[148:149], 1.0 op_sel_hi:[1,0]
	v_pk_fma_f32 v[6:7], v[146:147], v[6:7], v[178:179]
	v_pk_fma_f32 v[8:9], v[148:149], v[8:9], v[180:181]
	v_cvt_pk_bf16_f32 v6, v6, v7
	v_cvt_pk_bf16_f32 v7, v8, v9
	global_store_dwordx2 v[38:39], v[6:7], off offset:3072
	v_pk_add_f32 v[150:151], v[150:151], 1.0 op_sel_hi:[1,0]
	v_pk_add_f32 v[152:153], v[152:153], 1.0 op_sel_hi:[1,0]
	v_pk_fma_f32 v[2:3], v[150:151], v[2:3], v[182:183]
	v_pk_fma_f32 v[4:5], v[152:153], v[4:5], v[184:185]
	v_cvt_pk_bf16_f32 v2, v2, v3
	v_cvt_pk_bf16_f32 v3, v4, v5
	global_store_dwordx2 v[38:39], v[2:3], off offset:3584
	s_cmp_lg_u32 s21, 0
	s_cbranch_scc0 .LBB0_93
	s_min_i32 s10, s4, 0x4000
	s_ashr_i32 s10, s10, 11
	s_mul_hi_i32 s13, s10, 0xc000
	s_mul_i32 s10, s10, 0xc000
	s_add_u32 s12, s16, s10
	s_addc_u32 s13, s17, s13
	s_add_u32 s14, s12, 0x2000
	s_addc_u32 s15, s13, 0
	global_load_dwordx4 v[122:125], v1, s[14:15]
	global_load_dwordx4 v[126:129], v1, s[14:15] offset:1024
	global_load_dwordx4 v[130:133], v1, s[14:15] offset:2048
	global_load_dwordx4 v[134:137], v1, s[14:15] offset:3072
	global_load_dwordx4 v[138:141], v41, s[14:15]
	global_load_dwordx4 v[142:145], v42, s[14:15]
	global_load_dwordx4 v[146:149], v43, s[14:15]
	global_load_dwordx4 v[150:153], v44, s[14:15]
	global_load_dwordx4 v[154:157], v1, s[12:13]
	global_load_dwordx4 v[158:161], v1, s[12:13] offset:1024
	global_load_dwordx4 v[162:165], v1, s[12:13] offset:2048
	global_load_dwordx4 v[166:169], v1, s[12:13] offset:3072
	global_load_dwordx4 v[170:173], v41, s[12:13]
	global_load_dwordx4 v[174:177], v42, s[12:13]
	global_load_dwordx4 v[178:181], v43, s[12:13]
	global_load_dwordx4 v[182:185], v44, s[12:13]
	v_mov_b32_e32 v40, 0
	v_mov_b32_e32 v84, 0
	s_lshl_b64 s[2:3], s[4:5], 12
	s_add_u32 s4, s4, s0
	s_addc_u32 s5, s5, s1
	s_add_u32 s6, s6, s8
	s_addc_u32 s7, s7, s9
	s_cmpk_lt_i32 s4, 0x4800
	s_cselect_b32 s21, 1, 0
	s_cbranch_scc0 .Lp1_last_b
	s_cmpk_lt_i32 s4, 0x4000
	s_mov_b64 s[24:25], s[6:7]
	s_cbranch_scc1 .Lp1_lat_b2
	s_add_i32 s26, s4, 0xffffc000
	s_mov_b32 s27, 0
	s_lshl_b64 s[26:27], s[26:27], 13
	s_add_u32 s24, s72, s26
	s_addc_u32 s25, s73, s27
.Lp1_lat_b2:
	global_load_dwordx4 v[50:53], v1, s[24:25] nt
	global_load_dwordx4 v[54:57], v1, s[24:25] offset:1024 nt
	global_load_dwordx4 v[22:25], v1, s[24:25] offset:2048 nt
	global_load_dwordx4 v[18:21], v1, s[24:25] offset:3072 nt
	global_load_dwordx4 v[14:17], v41, s[24:25] nt
	global_load_dwordx4 v[10:13], v42, s[24:25] nt
	global_load_dwordx4 v[6:9], v43, s[24:25] nt
	global_load_dwordx4 v[2:5], v44, s[24:25] nt
	s_waitcnt vmcnt(24)
	s_branch .Lp1_red_b

; __device__ __forceinline__ void phase1(const Args& a, int lane, int wave, int vcu, int G) {
;     ...
;         for (int j = 0; j < 8; ++j) { v[j] = __builtin_nontemporal_load((const f32x4*)(xr + 4 * (lane + 64 * j))); ss += v[j][0] * v[j][0] + v[j][1] * v[j][1] + v[j][2] * v[j][2] + v[j][3] * v[j][3]; }
;         const float rstd = rsqrtf(wave_sum(ss) * (1.f / 2048.f) + EPS);
; #pragma unroll
;         for (int j = 0; j < 8; ++j) { const int c = 4 * (lane + 64 * j); const f32x4 gg = *(const f32x4*)(g + c), sh = *(const f32x4*)(mr + c), sc = *(const f32x4*)(mr + 2048 + c);
;             const f32x4 o = v[j] * rstd * gg * (sc + 1.f) + sh;
.Lp1_red_b:
	v_mul_f32_e32 v85, v186, v186
	v_mul_f32_e32 v86, v190, v190
	v_mul_f32_e32 v87, v194, v194
	v_mul_f32_e32 v88, v198, v198
	v_fmac_f32_e32 v85, v187, v187
	v_fmac_f32_e32 v86, v191, v191
	v_fmac_f32_e32 v87, v195, v195
	v_fmac_f32_e32 v88, v199, v199
	v_fmac_f32_e32 v85, v188, v188
	v_fmac_f32_e32 v86, v192, v192
	v_fmac_f32_e32 v87, v196, v196
	v_fmac_f32_e32 v88, v200, v200
	v_fmac_f32_e32 v85, v189, v189
	v_fmac_f32_e32 v86, v193, v193
	v_fmac_f32_e32 v87, v197, v197
	v_fmac_f32_e32 v88, v201, v201
	v_fmac_f32_e32 v85, v202, v202
	v_fmac_f32_e32 v86, v206, v206
	v_fmac_f32_e32 v87, v210, v210
	v_fmac_f32_e32 v88, v214, v214
	v_fmac_f32_e32 v85, v203, v203
	v_fmac_f32_e32 v86, v207, v207
	v_fmac_f32_e32 v87, v211, v211
	v_fmac_f32_e32 v88, v215, v215
	v_fmac_f32_e32 v85, v204, v204
	v_fmac_f32_e32 v86, v208, v208
	v_fmac_f32_e32 v87, v212, v212
	v_fmac_f32_e32 v88, v216, v216
	v_fmac_f32_e32 v85, v205, v205
	v_fmac_f32_e32 v86, v209, v209
	v_fmac_f32_e32 v87, v213, v213
	v_fmac_f32_e32 v88, v217, v217
	v_add_f32_e32 v85, v85, v86
	v_add_f32_e32 v87, v87, v88
	v_add_f32_e32 v38, v85, v87
	s_nop 1
	v_add_f32_dpp v38, v38, v38 row_shr:1 row_mask:0xf bank_mask:0xf bound_ctrl:1
	s_nop 1
	v_add_f32_dpp v38, v38, v38 row_shr:2 row_mask:0xf bank_mask:0xf bound_ctrl:1
	s_nop 1
	v_add_f32_dpp v38, v38, v38 row_shr:4 row_mask:0xf bank_mask:0xf bound_ctrl:1
	s_nop 1
	v_add_f32_dpp v38, v38, v38 row_shr:8 row_mask:0xf bank_mask:0xf bound_ctrl:1
	s_nop 1
	v_mov_b32_dpp v40, v38 row_bcast:15 row_mask:0xa bank_mask:0xf
	v_add_f32_e32 v38, v38, v40
	s_nop 1
	v_mov_b32_dpp v84, v38 row_bcast:31 row_mask:0xc bank_mask:0xf
	v_add_f32_e32 v38, v38, v84
	s_nop 0
	v_readlane_b32 s10, v38, 63
	s_nop 1
	v_fma_f32 v38, s10, v46, v45
	v_mul_f32_e32 v39, 0x4b800000, v38
	v_cmp_gt_f32_e32 vcc, s18, v38
	s_nop 1
	v_cndmask_b32_e32 v38, v38, v39, vcc
	v_rsq_f32_e32 v40, v38
	v_lshl_add_u64 v[38:39], v[36:37], 0, s[2:3]
	v_mul_f32_e32 v70, 0x45800000, v40
	v_cndmask_b32_e32 v40, v40, v70, vcc
	v_pk_mul_f32 v[186:187], v[186:187], v[40:41] op_sel_hi:[1,0]
	v_pk_mul_f32 v[188:189], v[188:189], v[40:41] op_sel_hi:[1,0]
	v_pk_mul_f32 v[190:191], v[190:191], v[40:41] op_sel_hi:[1,0]
	v_pk_mul_f32 v[192:193], v[192:193], v[40:41] op_sel_hi:[1,0]
	v_pk_mul_f32 v[194:195], v[194:195], v[40:41] op_sel_hi:[1,0]
	v_pk_mul_f32 v[196:197], v[196:197], v[40:41] op_sel_hi:[1,0]
	v_pk_mul_f32 v[198:199], v[198:199], v[40:41] op_sel_hi:[1,0]
	v_pk_mul_f32 v[200:201], v[200:201], v[40:41] op_sel_hi:[1,0]
	v_pk_mul_f32 v[202:203], v[202:203], v[40:41] op_sel_hi:[1,0]
	v_pk_mul_f32 v[204:205], v[204:205], v[40:41] op_sel_hi:[1,0]
	v_pk_mul_f32 v[206:207], v[206:207], v[40:41] op_sel_hi:[1,0]
	v_pk_mul_f32 v[208:209], v[208:209], v[40:41] op_sel_hi:[1,0]
	v_pk_mul_f32 v[210:211], v[210:211], v[40:41] op_sel_hi:[1,0]
	v_pk_mul_f32 v[212:213], v[212:213], v[40:41] op_sel_hi:[1,0]
	v_pk_mul_f32 v[214:215], v[214:215], v[40:41] op_sel_hi:[1,0]
	v_pk_mul_f32 v[216:217], v[216:217], v[40:41] op_sel_hi:[1,0]
	v_pk_mul_f32 v[186:187], v[90:91], v[186:187]
	v_pk_mul_f32 v[188:189], v[92:93], v[188:189]
	v_pk_mul_f32 v[190:191], v[94:95], v[190:191]
	v_pk_mul_f32 v[192:193], v[96:97], v[192:193]
	v_pk_mul_f32 v[194:195], v[98:99], v[194:195]
	v_pk_mul_f32 v[196:197], v[100:101], v[196:197]
	v_pk_mul_f32 v[198:199], v[102:103], v[198:199]
	v_pk_mul_f32 v[200:201], v[104:105], v[200:201]
	v_pk_mul_f32 v[202:203], v[106:107], v[202:203]
	v_pk_mul_f32 v[204:205], v[108:109], v[204:205]
	v_pk_mul_f32 v[206:207], v[110:111], v[206:207]
	v_pk_mul_f32 v[208:209], v[112:113], v[208:209]
	v_pk_mul_f32 v[210:211], v[114:115], v[210:211]
	v_pk_mul_f32 v[212:213], v[116:117], v[212:213]
	v_pk_mul_f32 v[214:215], v[118:119], v[214:215]
	v_pk_mul_f32 v[216:217], v[120:121], v[216:217]
	s_cmp_lg_u32 s21, 0
	s_cbranch_scc1 .Lp1_w8_b
	s_waitcnt vmcnt(0)
	s_branch .Lp1_mod_b

; __device__ __forceinline__ unsigned pk2(float lo, float hi) { return f2bf(lo) | (f2bf(hi) << 16); }
; __device__ __forceinline__ void phase1(const Args& a, int lane, int wave, int vcu, int G) {
;     ...
;         for (int j = 0; j < 8; ++j) { const int c = 4 * (lane + 64 * j); const f32x4 gg = *(const f32x4*)(g + c), sh = *(const f32x4*)(mr + c), sc = *(const f32x4*)(mr + 2048 + c);
;             const f32x4 o = v[j] * rstd * gg * (sc + 1.f) + sh;
;             v2u q; q.x = pk2(o[0], o[1]); q.y = pk2(o[2], o[3]); *(v2u*)(H + (size_t)m * 2048 + c) = q; }
.Lp1_mod_b:
	v_pk_add_f32 v[122:123], v[122:123], 1.0 op_sel_hi:[1,0]
	v_pk_add_f32 v[124:125], v[124:125], 1.0 op_sel_hi:[1,0]
	v_pk_fma_f32 v[186:187], v[122:123], v[186:187], v[154:155]
	v_pk_fma_f32 v[188:189], v[124:125], v[188:189], v[156:157]
	v_cvt_pk_bf16_f32 v186, v186, v187
	v_cvt_pk_bf16_f32 v187, v188, v189
	global_store_dwordx2 v[38:39], v[186:187], off
	v_pk_add_f32 v[126:127], v[126:127], 1.0 op_sel_hi:[1,0]
	v_pk_add_f32 v[128:129], v[128:129], 1.0 op_sel_hi:[1,0]
	v_pk_fma_f32 v[190:191], v[126:127], v[190:191], v[158:159]
	v_pk_fma_f32 v[192:193], v[128:129], v[192:193], v[160:161]
	v_cvt_pk_bf16_f32 v190, v190, v191
	v_cvt_pk_bf16_f32 v191, v192, v193
	global_store_dwordx2 v[38:39], v[190:191], off offset:512
	v_pk_add_f32 v[130:131], v[130:131], 1.0 op_sel_hi:[1,0]
	v_pk_add_f32 v[132:133], v[132:133], 1.0 op_sel_hi:[1,0]
	v_pk_fma_f32 v[194:195], v[130:131], v[194:195], v[162:163]
	v_pk_fma_f32 v[196:197], v[132:133], v[196:197], v[164:165]
	v_cvt_pk_bf16_f32 v194, v194, v195
	v_cvt_pk_bf16_f32 v195, v196, v197
	global_store_dwordx2 v[38:39], v[194:195], off offset:1024
	v_pk_add_f32 v[134:135], v[134:135], 1.0 op_sel_hi:[1,0]
	v_pk_add_f32 v[136:137], v[136:137], 1.0 op_sel_hi:[1,0]
	v_pk_fma_f32 v[198:199], v[134:135], v[198:199], v[166:167]
	v_pk_fma_f32 v[200:201], v[136:137], v[200:201], v[168:169]
	v_cvt_pk_bf16_f32 v198, v198, v199
	v_cvt_pk_bf16_f32 v199, v200, v201
	global_store_dwordx2 v[38:39], v[198:199], off offset:1536
	v_pk_add_f32 v[138:139], v[138:139], 1.0 op_sel_hi:[1,0]
	v_pk_add_f32 v[140:141], v[140:141], 1.0 op_sel_hi:[1,0]
	v_pk_fma_f32 v[202:203], v[138:139], v[202:203], v[170:171]
	v_pk_fma_f32 v[204:205], v[140:141], v[204:205], v[172:173]
	v_cvt_pk_bf16_f32 v202, v202, v203
	v_cvt_pk_bf16_f32 v203, v204, v205
	global_store_dwordx2 v[38:39], v[202:203], off offset:2048
	v_pk_add_f32 v[142:143], v[142:143], 1.0 op_sel_hi:[1,0]
	v_pk_add_f32 v[144:145], v[144:145], 1.0 op_sel_hi:[1,0]
	v_pk_fma_f32 v[206:207], v[142:143], v[206:207], v[174:175]
	v_pk_fma_f32 v[208:209], v[144:145], v[208:209], v[176:177]
	v_cvt_pk_bf16_f32 v206, v206, v207
	v_cvt_pk_bf16_f32 v207, v208, v209
	global_store_dwordx2 v[38:39], v[206:207], off offset:2560
	v_pk_add_f32 v[146:147], v[146:147], 1.0 op_sel_hi:[1,0]
	v_pk_add_f32 v[148:149], v[148:149], 1.0 op_sel_hi:[1,0]
	v_pk_fma_f32 v[210:211], v[146:147], v[210:211], v[178:179]
	v_pk_fma_f32 v[212:213], v[148:149], v[212:213], v[180:181]
	v_cvt_pk_bf16_f32 v210, v210, v211
	v_cvt_pk_bf16_f32 v211, v212, v213
	global_store_dwordx2 v[38:39], v[210:211], off offset:3072
	v_pk_add_f32 v[150:151], v[150:151], 1.0 op_sel_hi:[1,0]
	v_pk_add_f32 v[152:153], v[152:153], 1.0 op_sel_hi:[1,0]
	v_pk_fma_f32 v[214:215], v[150:151], v[214:215], v[182:183]
	v_pk_fma_f32 v[216:217], v[152:153], v[216:217], v[184:185]
	v_cvt_pk_bf16_f32 v214, v214, v215
	v_cvt_pk_bf16_f32 v215, v216, v217
	global_store_dwordx2 v[38:39], v[214:215], off offset:3584
	s_cmp_lg_u32 s21, 0
	s_cbranch_scc0 .LBB0_93
	s_branch .Lp1_top
